# stack + ROWSCALE GEMM epilogues: per-row rms scales loaded at unit start into K-loop-untouched VGPRs, epilogue vmcnt(0) drain removed
# speedup vs baseline: 1.0480x; 1.0020x over previous
.LBB0_1478:
	s_ashr_i32 s19, s18, 31
	s_lshl_b64 s[22:23], s[18:19], 20
	s_add_u32 s22, s20, s22
	s_addc_u32 s23, s21, s23
	s_and_b64 s[24:25], s[8:9], exec
	s_cselect_b32 s19, s23, s29
	s_cselect_b32 s27, s22, s28
	s_ashr_i32 s17, s16, 31
	s_lshl_b64 s[24:25], s[16:17], 20
	s_add_u32 s24, s15, s24
	s_addc_u32 s25, s33, s25
	s_and_b64 s[34:35], s[8:9], exec
	s_cselect_b32 s17, s25, s31
	s_cselect_b32 s51, s24, s30
	s_lshl_b32 s34, s26, 8
	s_ashr_i32 s35, s34, 31
	v_lshl_add_u64 v[238:239], s[34:35], 2, v[138:139]
	global_load_dword v240, v[238:239], off
	global_load_dword v242, v[238:239], off offset:64
	global_load_dword v244, v[238:239], off offset:128
	global_load_dword v246, v[238:239], off offset:192
	global_load_dword v248, v[238:239], off offset:512
	global_load_dword v250, v[238:239], off offset:576
	global_load_dword v252, v[238:239], off offset:640
	global_load_dword v238, v[238:239], off offset:704
	s_add_u32 s28, s28, 0x80080
	s_addc_u32 s29, s29, 0
	s_add_u32 s52, s30, 0x100
	s_addc_u32 s53, s31, 0
	s_mov_b32 s54, -2
	s_waitcnt vmcnt(0)
	ds_read_b128 v[154:157], v150
	ds_read_b128 v[158:161], v150 offset:1024
	ds_read_b128 v[162:165], v150 offset:2048
	ds_read_b128 v[166:169], v150 offset:3072
	ds_read_b128 v[170:173], v151
	ds_read_b128 v[174:177], v151 offset:1024
	ds_read_b128 v[178:181], v151 offset:2048
	ds_read_b128 v[182:185], v151 offset:3072
	s_add_u32 s30, s28, 0xfff80080
	s_addc_u32 s31, s29, -1
	s_cmp_eq_u32 s54, 28
	s_cselect_b32 s35, s19, s31
	s_cselect_b32 s34, s27, s30
	s_cselect_b32 s31, s17, s53
	s_cselect_b32 s30, s51, s52
	v_lshl_add_u64 v[218:219], s[28:29], 0, v[140:141]
	s_add_i32 m0, s39, 0xc000
	ds_read_b128 v[186:189], v152
	ds_read_b128 v[190:193], v152 offset:1024
	ds_read_b128 v[194:197], v152 offset:2048
	ds_read_b128 v[198:201], v152 offset:3072
	ds_read_b128 v[202:205], v152 offset:4096
	ds_read_b128 v[206:209], v152 offset:5120
	ds_read_b128 v[210:213], v152 offset:6144
	ds_read_b128 v[214:217], v152 offset:7168
	global_load_lds_dwordx4 v[218:219], off
	v_lshl_add_u64 v[218:219], s[28:29], 0, v[142:143]
	s_add_i32 m0, s39, 0xe000
	s_nop 0
	global_load_lds_dwordx4 v[218:219], off
	s_waitcnt vmcnt(8)
	s_waitcnt lgkmcnt(0)
	s_setprio 1
	s_barrier
	v_mfma_f32_16x16x32_bf16 v[126:129], v[154:157], v[186:189], 0
	v_mfma_f32_16x16x32_bf16 v[122:125], v[162:165], v[186:189], 0
	v_mfma_f32_16x16x32_bf16 v[118:121], v[154:157], v[194:197], 0
	v_mfma_f32_16x16x32_bf16 v[114:117], v[162:165], v[194:197], 0
	v_mfma_f32_16x16x32_bf16 v[110:113], v[154:157], v[202:205], 0
	v_mfma_f32_16x16x32_bf16 v[102:105], v[162:165], v[202:205], 0
	v_mfma_f32_16x16x32_bf16 v[94:97], v[154:157], v[210:213], 0
	v_mfma_f32_16x16x32_bf16 v[86:89], v[162:165], v[210:213], 0
	v_mfma_f32_16x16x32_bf16 v[126:129], v[158:161], v[190:193], v[126:129]
	v_mfma_f32_16x16x32_bf16 v[122:125], v[166:169], v[190:193], v[122:125]
	v_mfma_f32_16x16x32_bf16 v[118:121], v[158:161], v[198:201], v[118:121]
	v_mfma_f32_16x16x32_bf16 v[114:117], v[166:169], v[198:201], v[114:117]
	v_mfma_f32_16x16x32_bf16 v[110:113], v[158:161], v[206:209], v[110:113]
	v_mfma_f32_16x16x32_bf16 v[102:105], v[166:169], v[206:209], v[102:105]
	v_mfma_f32_16x16x32_bf16 v[94:97], v[158:161], v[214:217], v[94:97]
	v_mfma_f32_16x16x32_bf16 v[86:89], v[166:169], v[214:217], v[86:89]
	s_setprio 0
	s_setprio 1
	v_mfma_f32_16x16x32_bf16 v[106:109], v[170:173], v[186:189], 0
	v_mfma_f32_16x16x32_bf16 v[98:101], v[178:181], v[186:189], 0
	v_mfma_f32_16x16x32_bf16 v[90:93], v[170:173], v[194:197], 0
	v_mfma_f32_16x16x32_bf16 v[82:85], v[178:181], v[194:197], 0
	v_mfma_f32_16x16x32_bf16 v[78:81], v[170:173], v[202:205], 0
	v_mfma_f32_16x16x32_bf16 v[74:77], v[178:181], v[202:205], 0
	v_mfma_f32_16x16x32_bf16 v[70:73], v[170:173], v[210:213], 0
	v_mfma_f32_16x16x32_bf16 v[66:69], v[178:181], v[210:213], 0
	v_mfma_f32_16x16x32_bf16 v[106:109], v[174:177], v[190:193], v[106:109]
	v_mfma_f32_16x16x32_bf16 v[98:101], v[182:185], v[190:193], v[98:101]
	v_mfma_f32_16x16x32_bf16 v[90:93], v[174:177], v[198:201], v[90:93]
	v_mfma_f32_16x16x32_bf16 v[82:85], v[182:185], v[198:201], v[82:85]
	v_mfma_f32_16x16x32_bf16 v[78:81], v[174:177], v[206:209], v[78:81]
	v_mfma_f32_16x16x32_bf16 v[74:77], v[182:185], v[206:209], v[74:77]
	v_mfma_f32_16x16x32_bf16 v[70:73], v[174:177], v[214:217], v[70:73]
	v_mfma_f32_16x16x32_bf16 v[66:69], v[182:185], v[214:217], v[66:69]
	s_barrier
	s_setprio 0
	s_add_i32 s55, s47, s36
	v_lshl_add_u64 v[218:219], s[30:31], 0, v[134:135]
	s_mov_b32 m0, s55
	ds_read_b128 v[186:189], v152 offset:16384
	ds_read_b128 v[190:193], v152 offset:17408
	ds_read_b128 v[194:197], v152 offset:18432
	ds_read_b128 v[198:201], v152 offset:19456
	ds_read_b128 v[202:205], v152 offset:20480
	ds_read_b128 v[206:209], v152 offset:21504
	ds_read_b128 v[210:213], v152 offset:22528
	ds_read_b128 v[214:217], v152 offset:23552
	global_load_lds_dwordx4 v[218:219], off
	s_add_i32 m0, s55, 0x2000
	s_add_u32 s56, s30, 0x80000
	v_lshl_add_u64 v[220:221], s[30:31], 0, v[130:131]
	s_addc_u32 s57, s31, 0
	s_add_i32 s55, s48, s36
	global_load_lds_dwordx4 v[220:221], off
	v_lshl_add_u64 v[222:223], s[56:57], 0, v[134:135]
	s_mov_b32 m0, s55
	v_lshl_add_u64 v[224:225], s[34:35], 0, v[132:133]
	global_load_lds_dwordx4 v[222:223], off
	v_lshl_add_u64 v[222:223], s[56:57], 0, v[130:131]
	s_add_i32 m0, s55, 0x2000
	s_nop 0
	global_load_lds_dwordx4 v[222:223], off
	v_lshl_add_u64 v[222:223], s[34:35], 0, v[136:137]
	s_mov_b32 m0, s39
	s_nop 0
	global_load_lds_dwordx4 v[222:223], off
	s_mov_b32 m0, s40
	s_nop 0
	global_load_lds_dwordx4 v[224:225], off
	s_waitcnt vmcnt(8)
	s_waitcnt lgkmcnt(0)
	s_setprio 1
	s_barrier
	v_mfma_f32_16x16x32_bf16 v[62:65], v[154:157], v[186:189], 0
	v_mfma_f32_16x16x32_bf16 v[58:61], v[162:165], v[186:189], 0
	v_mfma_f32_16x16x32_bf16 v[54:57], v[154:157], v[194:197], 0
	v_mfma_f32_16x16x32_bf16 v[50:53], v[162:165], v[194:197], 0
	v_mfma_f32_16x16x32_bf16 v[46:49], v[154:157], v[202:205], 0
	v_mfma_f32_16x16x32_bf16 v[38:41], v[162:165], v[202:205], 0
	v_mfma_f32_16x16x32_bf16 v[30:33], v[154:157], v[210:213], 0
	v_mfma_f32_16x16x32_bf16 v[22:25], v[162:165], v[210:213], 0
	v_mfma_f32_16x16x32_bf16 v[62:65], v[158:161], v[190:193], v[62:65]
	v_mfma_f32_16x16x32_bf16 v[58:61], v[166:169], v[190:193], v[58:61]
	v_mfma_f32_16x16x32_bf16 v[54:57], v[158:161], v[198:201], v[54:57]
	v_mfma_f32_16x16x32_bf16 v[50:53], v[166:169], v[198:201], v[50:53]
	v_mfma_f32_16x16x32_bf16 v[46:49], v[158:161], v[206:209], v[46:49]
	v_mfma_f32_16x16x32_bf16 v[38:41], v[166:169], v[206:209], v[38:41]
	v_mfma_f32_16x16x32_bf16 v[30:33], v[158:161], v[214:217], v[30:33]
	v_mfma_f32_16x16x32_bf16 v[22:25], v[166:169], v[214:217], v[22:25]
	s_setprio 0
	s_setprio 1
	v_mfma_f32_16x16x32_bf16 v[42:45], v[170:173], v[186:189], 0
	v_mfma_f32_16x16x32_bf16 v[34:37], v[178:181], v[186:189], 0
	v_mfma_f32_16x16x32_bf16 v[26:29], v[170:173], v[194:197], 0
	v_mfma_f32_16x16x32_bf16 v[18:21], v[178:181], v[194:197], 0
	v_mfma_f32_16x16x32_bf16 v[14:17], v[170:173], v[202:205], 0
	v_mfma_f32_16x16x32_bf16 v[10:13], v[178:181], v[202:205], 0
	v_mfma_f32_16x16x32_bf16 v[6:9], v[170:173], v[210:213], 0
	v_mfma_f32_16x16x32_bf16 v[2:5], v[178:181], v[210:213], 0
	v_mfma_f32_16x16x32_bf16 v[42:45], v[174:177], v[190:193], v[42:45]
	v_mfma_f32_16x16x32_bf16 v[34:37], v[182:185], v[190:193], v[34:37]
	v_mfma_f32_16x16x32_bf16 v[26:29], v[174:177], v[198:201], v[26:29]
	v_mfma_f32_16x16x32_bf16 v[18:21], v[182:185], v[198:201], v[18:21]
	v_mfma_f32_16x16x32_bf16 v[14:17], v[174:177], v[206:209], v[14:17]
	v_mfma_f32_16x16x32_bf16 v[10:13], v[182:185], v[206:209], v[10:13]
	v_mfma_f32_16x16x32_bf16 v[6:9], v[174:177], v[214:217], v[6:9]
	v_mfma_f32_16x16x32_bf16 v[2:5], v[182:185], v[214:217], v[2:5]
	s_barrier
	s_setprio 0
	s_add_i32 s55, 0, 0x18000
	v_add_u32_e32 v153, s55, v148
	s_add_i32 s56, 0, 0x1c000
	ds_read_b128 v[154:157], v153
	ds_read_b128 v[158:161], v153 offset:1024
	ds_read_b128 v[162:165], v153 offset:2048
	ds_read_b128 v[166:169], v153 offset:3072
	v_add_u32_e32 v153, s56, v148
	ds_read_b128 v[170:173], v153
	ds_read_b128 v[174:177], v153 offset:1024
	ds_read_b128 v[178:181], v153 offset:2048
	ds_read_b128 v[182:185], v153 offset:3072
	s_add_u32 s34, s34, 0x80000
	s_addc_u32 s35, s35, 0
	s_mov_b32 m0, s41
	v_lshl_add_u64 v[226:227], s[34:35], 0, v[136:137]
	ds_read_b128 v[186:189], v152 offset:32768
	ds_read_b128 v[190:193], v152 offset:33792
	ds_read_b128 v[194:197], v152 offset:34816
	ds_read_b128 v[198:201], v152 offset:35840
	ds_read_b128 v[202:205], v152 offset:36864
	ds_read_b128 v[206:209], v152 offset:37888
	ds_read_b128 v[210:213], v152 offset:38912
	ds_read_b128 v[214:217], v152 offset:39936
	global_load_lds_dwordx4 v[226:227], off
	v_lshl_add_u64 v[226:227], s[34:35], 0, v[132:133]
	s_mov_b32 m0, s42
	s_nop 0
	global_load_lds_dwordx4 v[226:227], off
	s_waitcnt vmcnt(8)
	s_waitcnt lgkmcnt(0)
	s_setprio 1
	s_barrier
	v_mfma_f32_16x16x32_bf16 v[126:129], v[154:157], v[186:189], v[126:129]
	v_mfma_f32_16x16x32_bf16 v[122:125], v[162:165], v[186:189], v[122:125]
	v_mfma_f32_16x16x32_bf16 v[118:121], v[154:157], v[194:197], v[118:121]
	v_mfma_f32_16x16x32_bf16 v[114:117], v[162:165], v[194:197], v[114:117]
	v_mfma_f32_16x16x32_bf16 v[110:113], v[154:157], v[202:205], v[110:113]
	v_mfma_f32_16x16x32_bf16 v[102:105], v[162:165], v[202:205], v[102:105]
	v_mfma_f32_16x16x32_bf16 v[94:97], v[154:157], v[210:213], v[94:97]
	v_mfma_f32_16x16x32_bf16 v[86:89], v[162:165], v[210:213], v[86:89]
	v_mfma_f32_16x16x32_bf16 v[126:129], v[158:161], v[190:193], v[126:129]
	v_mfma_f32_16x16x32_bf16 v[122:125], v[166:169], v[190:193], v[122:125]
	v_mfma_f32_16x16x32_bf16 v[118:121], v[158:161], v[198:201], v[118:121]
	v_mfma_f32_16x16x32_bf16 v[114:117], v[166:169], v[198:201], v[114:117]
	v_mfma_f32_16x16x32_bf16 v[110:113], v[158:161], v[206:209], v[110:113]
	v_mfma_f32_16x16x32_bf16 v[102:105], v[166:169], v[206:209], v[102:105]
	v_mfma_f32_16x16x32_bf16 v[94:97], v[158:161], v[214:217], v[94:97]
	v_mfma_f32_16x16x32_bf16 v[86:89], v[166:169], v[214:217], v[86:89]
	s_setprio 0
	s_setprio 1
	v_mfma_f32_16x16x32_bf16 v[106:109], v[170:173], v[186:189], v[106:109]
	v_mfma_f32_16x16x32_bf16 v[98:101], v[178:181], v[186:189], v[98:101]
	v_mfma_f32_16x16x32_bf16 v[90:93], v[170:173], v[194:197], v[90:93]
	v_mfma_f32_16x16x32_bf16 v[82:85], v[178:181], v[194:197], v[82:85]
	v_mfma_f32_16x16x32_bf16 v[78:81], v[170:173], v[202:205], v[78:81]
	v_mfma_f32_16x16x32_bf16 v[74:77], v[178:181], v[202:205], v[74:77]
	v_mfma_f32_16x16x32_bf16 v[70:73], v[170:173], v[210:213], v[70:73]
	v_mfma_f32_16x16x32_bf16 v[66:69], v[178:181], v[210:213], v[66:69]
	v_mfma_f32_16x16x32_bf16 v[106:109], v[174:177], v[190:193], v[106:109]
	v_mfma_f32_16x16x32_bf16 v[98:101], v[182:185], v[190:193], v[98:101]
	v_mfma_f32_16x16x32_bf16 v[90:93], v[174:177], v[198:201], v[90:93]
	v_mfma_f32_16x16x32_bf16 v[82:85], v[182:185], v[198:201], v[82:85]
	v_mfma_f32_16x16x32_bf16 v[78:81], v[174:177], v[206:209], v[78:81]
	v_mfma_f32_16x16x32_bf16 v[74:77], v[182:185], v[206:209], v[74:77]
	v_mfma_f32_16x16x32_bf16 v[70:73], v[174:177], v[214:217], v[70:73]
	v_mfma_f32_16x16x32_bf16 v[66:69], v[182:185], v[214:217], v[66:69]
	s_barrier
	s_setprio 0
	s_add_i32 s34, s55, s36
	v_lshl_add_u64 v[218:219], v[218:219], 0, s[10:11]
	s_mov_b32 m0, s34
	ds_read_b128 v[186:189], v152 offset:49152
	ds_read_b128 v[190:193], v152 offset:50176
	ds_read_b128 v[194:197], v152 offset:51200
	ds_read_b128 v[198:201], v152 offset:52224
	ds_read_b128 v[202:205], v152 offset:53248
	ds_read_b128 v[206:209], v152 offset:54272
	ds_read_b128 v[210:213], v152 offset:55296
	ds_read_b128 v[214:217], v152 offset:56320
	global_load_lds_dwordx4 v[218:219], off
	s_add_i32 m0, s34, 0x2000
	s_add_u32 s30, s30, 0x80080
	v_lshl_add_u64 v[218:219], v[220:221], 0, s[10:11]
	s_addc_u32 s31, s31, 0
	s_add_i32 s34, s56, s36
	global_load_lds_dwordx4 v[218:219], off
	v_lshl_add_u64 v[218:219], s[30:31], 0, v[134:135]
	s_mov_b32 m0, s34
	s_nop 0
	global_load_lds_dwordx4 v[218:219], off
	v_lshl_add_u64 v[218:219], s[30:31], 0, v[130:131]
	s_add_i32 m0, s34, 0x2000
	s_nop 0
	global_load_lds_dwordx4 v[218:219], off
	v_lshl_add_u64 v[218:219], v[222:223], 0, s[10:11]
	s_mov_b32 m0, s44
	s_nop 0
	global_load_lds_dwordx4 v[218:219], off
	v_lshl_add_u64 v[218:219], v[224:225], 0, s[10:11]
	s_mov_b32 m0, s45
	s_nop 0
	global_load_lds_dwordx4 v[218:219], off
	s_waitcnt vmcnt(8)
	s_waitcnt lgkmcnt(0)
	s_setprio 1
	s_barrier
	v_mfma_f32_16x16x32_bf16 v[62:65], v[154:157], v[186:189], v[62:65]
	v_mfma_f32_16x16x32_bf16 v[58:61], v[162:165], v[186:189], v[58:61]
	v_mfma_f32_16x16x32_bf16 v[54:57], v[154:157], v[194:197], v[54:57]
	v_mfma_f32_16x16x32_bf16 v[50:53], v[162:165], v[194:197], v[50:53]
	v_mfma_f32_16x16x32_bf16 v[46:49], v[154:157], v[202:205], v[46:49]
	v_mfma_f32_16x16x32_bf16 v[38:41], v[162:165], v[202:205], v[38:41]
	v_mfma_f32_16x16x32_bf16 v[30:33], v[154:157], v[210:213], v[30:33]
	v_mfma_f32_16x16x32_bf16 v[22:25], v[162:165], v[210:213], v[22:25]
	v_mfma_f32_16x16x32_bf16 v[62:65], v[158:161], v[190:193], v[62:65]
	v_mfma_f32_16x16x32_bf16 v[58:61], v[166:169], v[190:193], v[58:61]
	v_mfma_f32_16x16x32_bf16 v[54:57], v[158:161], v[198:201], v[54:57]
	v_mfma_f32_16x16x32_bf16 v[50:53], v[166:169], v[198:201], v[50:53]
	v_mfma_f32_16x16x32_bf16 v[46:49], v[158:161], v[206:209], v[46:49]
	v_mfma_f32_16x16x32_bf16 v[38:41], v[166:169], v[206:209], v[38:41]
	v_mfma_f32_16x16x32_bf16 v[30:33], v[158:161], v[214:217], v[30:33]
	v_mfma_f32_16x16x32_bf16 v[22:25], v[166:169], v[214:217], v[22:25]
	s_setprio 0
	s_setprio 1
	v_mfma_f32_16x16x32_bf16 v[42:45], v[170:173], v[186:189], v[42:45]
	v_mfma_f32_16x16x32_bf16 v[34:37], v[178:181], v[186:189], v[34:37]
	v_mfma_f32_16x16x32_bf16 v[26:29], v[170:173], v[194:197], v[26:29]
	v_mfma_f32_16x16x32_bf16 v[18:21], v[178:181], v[194:197], v[18:21]
	v_mfma_f32_16x16x32_bf16 v[14:17], v[170:173], v[202:205], v[14:17]
	v_mfma_f32_16x16x32_bf16 v[10:13], v[178:181], v[202:205], v[10:13]
	v_mfma_f32_16x16x32_bf16 v[6:9], v[170:173], v[210:213], v[6:9]
	v_mfma_f32_16x16x32_bf16 v[2:5], v[178:181], v[210:213], v[2:5]
	v_mfma_f32_16x16x32_bf16 v[42:45], v[174:177], v[190:193], v[42:45]
	v_mfma_f32_16x16x32_bf16 v[34:37], v[182:185], v[190:193], v[34:37]
	v_mfma_f32_16x16x32_bf16 v[26:29], v[174:177], v[198:201], v[26:29]
	v_mfma_f32_16x16x32_bf16 v[18:21], v[182:185], v[198:201], v[18:21]
	v_mfma_f32_16x16x32_bf16 v[14:17], v[174:177], v[206:209], v[14:17]
	v_mfma_f32_16x16x32_bf16 v[10:13], v[182:185], v[206:209], v[10:13]
	v_mfma_f32_16x16x32_bf16 v[6:9], v[174:177], v[214:217], v[6:9]
	v_mfma_f32_16x16x32_bf16 v[2:5], v[182:185], v[214:217], v[2:5]
	s_barrier
	s_setprio 0
	s_add_i32 s54, s54, 2
	s_add_u32 s28, s28, 0x100
	s_addc_u32 s29, s29, 0
	s_add_u32 s52, s52, 0x100
	s_addc_u32 s53, s53, 0
	s_cmp_gt_u32 s54, 29

.LBB0_1482:
	s_lshl_b32 s26, s26, 8
	s_ashr_i32 s27, s26, 31
	v_lshl_add_u64 v[154:155], s[26:27], 2, v[138:139]
	v_mov_b32_e32 v156, v240
	v_mov_b32_e32 v158, v242
	v_mov_b32_e32 v160, v244
	v_mov_b32_e32 v162, v246
	v_mov_b32_e32 v164, v248
	v_mov_b32_e32 v166, v250
	v_mov_b32_e32 v168, v252
	s_nop 0
	v_mov_b32_e32 v154, v238
	v_lshl_or_b32 v170, s50, 7, v149
	v_add_u32_e32 v153, s26, v1
	v_ashrrev_i32_e32 v171, 31, v170
	s_andn2_b64 vcc, exec, s[8:9]
	s_mov_b64 s[8:9], -1
	v_pk_mul_f32 v[126:127], v[126:127], v[156:157] op_sel_hi:[1,0]
	v_pk_mul_f32 v[128:129], v[128:129], v[156:157] op_sel_hi:[1,0]
	v_pk_mul_f32 v[180:181], v[78:79], v[160:161] op_sel_hi:[1,0]
	v_pk_mul_f32 v[178:179], v[82:83], v[158:159] op_sel_hi:[1,0]
	v_pk_mul_f32 v[78:79], v[44:45], v[164:165] op_sel_hi:[1,0]
	v_pk_mul_f32 v[44:45], v[52:53], v[166:167] op_sel_hi:[1,0]
	v_pk_mul_f32 v[52:53], v[18:19], v[166:167] op_sel_hi:[1,0]
	v_pk_mul_f32 v[18:19], v[126:127], s[14:15] op_sel_hi:[1,0]
	v_pk_mul_f32 v[82:83], v[86:87], v[162:163] op_sel_hi:[1,0]
	v_pk_mul_f32 v[86:87], v[68:69], v[162:163] op_sel_hi:[1,0]
	v_pk_mul_f32 v[68:69], v[34:35], v[164:165] op_sel_hi:[1,0]
	v_pk_mul_f32 v[34:35], v[12:13], v[168:169] op_sel_hi:[1,0]
	v_pk_mul_f32 v[12:13], v[22:23], v[154:155] op_sel_hi:[1,0]
	v_pk_mul_f32 v[22:23], v[128:129], s[14:15] op_sel_hi:[1,0]
	v_exp_f32_e32 v18, v18
	v_exp_f32_e32 v19, v19
	v_exp_f32_e32 v22, v22
	v_exp_f32_e32 v23, v23
	v_pk_mul_f32 v[106:107], v[106:107], v[156:157] op_sel_hi:[1,0]
	v_pk_add_f32 v[18:19], v[18:19], 1.0 op_sel_hi:[1,0]
	v_pk_mul_f32 v[124:125], v[124:125], v[156:157] op_sel_hi:[1,0]
	v_pk_add_f32 v[22:23], v[22:23], 1.0 op_sel_hi:[1,0]
	v_rcp_f32_e32 v18, v18
	v_rcp_f32_e32 v19, v19
	v_rcp_f32_e32 v22, v22
	v_rcp_f32_e32 v23, v23
	v_pk_mul_f32 v[122:123], v[122:123], v[156:157] op_sel_hi:[1,0]
	v_pk_mul_f32 v[108:109], v[108:109], v[156:157] op_sel_hi:[1,0]
	v_pk_mul_f32 v[120:121], v[120:121], v[158:159] op_sel_hi:[1,0]
	v_pk_mul_f32 v[118:119], v[118:119], v[158:159] op_sel_hi:[1,0]
	v_pk_mul_f32 v[116:117], v[116:117], v[158:159] op_sel_hi:[1,0]
	v_pk_mul_f32 v[114:115], v[114:115], v[158:159] op_sel_hi:[1,0]
	v_pk_mul_f32 v[174:175], v[90:91], v[158:159] op_sel_hi:[1,0]
	v_pk_mul_f32 v[176:177], v[92:93], v[158:159] op_sel_hi:[1,0]
	v_pk_mul_f32 v[158:159], v[84:85], v[158:159] op_sel_hi:[1,0]
	v_pk_mul_f32 v[84:85], v[66:67], v[162:163] op_sel_hi:[1,0]
	v_pk_mul_f32 v[66:67], v[58:59], v[164:165] op_sel_hi:[1,0]
	v_pk_mul_f32 v[58:59], v[54:55], v[166:167] op_sel_hi:[1,0]
	v_pk_mul_f32 v[54:55], v[20:21], v[166:167] op_sel_hi:[1,0]
	v_pk_mul_f32 v[20:21], v[40:41], v[168:169] op_sel_hi:[1,0]
	v_pk_mul_f32 v[40:41], v[16:17], v[168:169] op_sel_hi:[1,0]
	v_pk_mul_f32 v[16:17], v[30:31], v[154:155] op_sel_hi:[1,0]
	v_pk_mul_f32 v[30:31], v[126:127], v[106:107]
	v_pk_mul_f32 v[172:173], v[98:99], v[156:157] op_sel_hi:[1,0]
	v_pk_mul_f32 v[156:157], v[100:101], v[156:157] op_sel_hi:[1,0]
	v_pk_mul_f32 v[100:101], v[102:103], v[160:161] op_sel_hi:[1,0]
	v_pk_mul_f32 v[102:103], v[74:75], v[160:161] op_sel_hi:[1,0]
	v_pk_mul_f32 v[92:93], v[94:95], v[162:163] op_sel_hi:[1,0]
	v_pk_mul_f32 v[94:95], v[72:73], v[162:163] op_sel_hi:[1,0]
	v_pk_mul_f32 v[72:73], v[64:65], v[164:165] op_sel_hi:[1,0]
	v_pk_mul_f32 v[74:75], v[62:63], v[164:165] op_sel_hi:[1,0]
	v_pk_mul_f32 v[64:65], v[60:61], v[164:165] op_sel_hi:[1,0]
	v_pk_mul_f32 v[60:61], v[26:27], v[166:167] op_sel_hi:[1,0]
	v_pk_mul_f32 v[62:63], v[28:29], v[166:167] op_sel_hi:[1,0]
	v_pk_mul_f32 v[26:27], v[38:39], v[168:169] op_sel_hi:[1,0]
	v_pk_mul_f32 v[38:39], v[14:15], v[168:169] op_sel_hi:[1,0]
	v_pk_mul_f32 v[28:29], v[10:11], v[168:169] op_sel_hi:[1,0]
	v_pk_mul_f32 v[14:15], v[32:33], v[154:155] op_sel_hi:[1,0]
	v_pk_mul_f32 v[10:11], v[24:25], v[154:155] op_sel_hi:[1,0]
	v_pk_mul_f32 v[24:25], v[128:129], v[108:109]
	v_pk_mul_f32 v[32:33], v[122:123], s[14:15] op_sel_hi:[1,0]
	v_pk_mul_f32 v[18:19], v[30:31], v[18:19]
	v_pk_mul_f32 v[30:31], v[124:125], s[14:15] op_sel_hi:[1,0]
	v_pk_mul_f32 v[22:23], v[24:25], v[22:23]
	v_exp_f32_e32 v24, v32
	v_exp_f32_e32 v25, v33
	v_exp_f32_e32 v30, v30
	v_exp_f32_e32 v31, v31
	v_pk_mul_f32 v[98:99], v[104:105], v[160:161] op_sel_hi:[1,0]
	v_pk_add_f32 v[24:25], v[24:25], 1.0 op_sel_hi:[1,0]
	v_pk_mul_f32 v[104:105], v[76:77], v[160:161] op_sel_hi:[1,0]
	v_pk_add_f32 v[30:31], v[30:31], 1.0 op_sel_hi:[1,0]
	v_rcp_f32_e32 v24, v24
	v_rcp_f32_e32 v25, v25
	v_rcp_f32_e32 v30, v30
	v_rcp_f32_e32 v31, v31
	v_pk_mul_f32 v[76:77], v[42:43], v[164:165] op_sel_hi:[1,0]
	v_pk_mul_f32 v[42:43], v[46:47], v[168:169] op_sel_hi:[1,0]
	v_pk_mul_f32 v[32:33], v[124:125], v[156:157]
	v_pk_mul_f32 v[46:47], v[122:123], v[172:173]
	v_pk_mul_f32 v[90:91], v[96:97], v[162:163] op_sel_hi:[1,0]
	v_pk_mul_f32 v[24:25], v[46:47], v[24:25]
	v_pk_mul_f32 v[46:47], v[32:33], v[30:31]
	v_cvt_pk_bf16_f32 v30, v18, v19
	v_mov_b64_e32 v[18:19], s[6:7]
	v_cvt_pk_bf16_f32 v31, v22, v23
	v_cvt_pk_bf16_f32 v32, v24, v25
	v_mad_i64_i32 v[24:25], s[26:27], v153, s49, v[18:19]
	v_lshlrev_b64 v[22:23], 1, v[170:171]
	v_lshl_add_u64 v[24:25], v[24:25], 0, v[22:23]
	v_cvt_pk_bf16_f32 v33, v46, v47
	global_store_dwordx4 v[24:25], v[30:33], off
	v_pk_mul_f32 v[24:25], v[118:119], s[14:15] op_sel_hi:[1,0]
	v_pk_mul_f32 v[46:47], v[118:119], v[174:175]
	v_pk_mul_f32 v[30:31], v[120:121], s[14:15] op_sel_hi:[1,0]
	v_exp_f32_e32 v24, v24
	v_exp_f32_e32 v30, v30
	v_exp_f32_e32 v31, v31
	v_exp_f32_e32 v25, v25
	v_pk_mul_f32 v[32:33], v[120:121], v[176:177]
	v_pk_mul_f32 v[96:97], v[114:115], v[178:179]
	v_pk_add_f32 v[30:31], v[30:31], 1.0 op_sel_hi:[1,0]
	v_pk_add_f32 v[24:25], v[24:25], 1.0 op_sel_hi:[1,0]
	v_rcp_f32_e32 v30, v30
	v_rcp_f32_e32 v31, v31
	v_rcp_f32_e32 v24, v24
	v_rcp_f32_e32 v25, v25
	v_pk_mul_f32 v[112:113], v[112:113], v[160:161] op_sel_hi:[1,0]
	v_pk_mul_f32 v[32:33], v[32:33], v[30:31]
	v_pk_mul_f32 v[30:31], v[114:115], s[14:15] op_sel_hi:[1,0]
	v_pk_mul_f32 v[24:25], v[46:47], v[24:25]
	v_exp_f32_e32 v30, v30
	v_exp_f32_e32 v31, v31
	v_pk_mul_f32 v[46:47], v[116:117], s[14:15] op_sel_hi:[1,0]
	v_pk_mul_f32 v[182:183], v[80:81], v[160:161] op_sel_hi:[1,0]
	v_exp_f32_e32 v46, v46
	v_exp_f32_e32 v47, v47
	v_pk_add_f32 v[30:31], v[30:31], 1.0 op_sel_hi:[1,0]
	v_pk_mul_f32 v[80:81], v[88:89], v[162:163] op_sel_hi:[1,0]
	v_rcp_f32_e32 v30, v30
	v_rcp_f32_e32 v31, v31
	v_pk_add_f32 v[46:47], v[46:47], 1.0 op_sel_hi:[1,0]
	v_pk_mul_f32 v[88:89], v[70:71], v[162:163] op_sel_hi:[1,0]
	v_rcp_f32_e32 v46, v46
	v_rcp_f32_e32 v47, v47
	v_pk_mul_f32 v[96:97], v[96:97], v[30:31]
	v_cvt_pk_bf16_f32 v30, v24, v25
	v_or_b32_e32 v24, 16, v153
	v_mad_i64_i32 v[24:25], s[26:27], v24, s49, v[18:19]
	v_pk_mul_f32 v[70:71], v[36:37], v[164:165] op_sel_hi:[1,0]
	v_pk_mul_f32 v[36:37], v[48:49], v[168:169] op_sel_hi:[1,0]
	v_pk_mul_f32 v[48:49], v[116:117], v[158:159]
	v_cvt_pk_bf16_f32 v31, v32, v33
	v_lshl_add_u64 v[24:25], v[24:25], 0, v[22:23]
	v_pk_mul_f32 v[46:47], v[48:49], v[46:47]
	v_cvt_pk_bf16_f32 v32, v96, v97
	v_pk_mul_f32 v[110:111], v[110:111], v[160:161] op_sel_hi:[1,0]
	v_cvt_pk_bf16_f32 v33, v46, v47
	global_store_dwordx4 v[24:25], v[30:33], off
	v_pk_mul_f32 v[24:25], v[110:111], s[14:15] op_sel_hi:[1,0]
	v_pk_mul_f32 v[46:47], v[110:111], v[180:181]
	v_pk_mul_f32 v[30:31], v[112:113], s[14:15] op_sel_hi:[1,0]
	v_exp_f32_e32 v24, v24
	v_exp_f32_e32 v30, v30
	v_exp_f32_e32 v31, v31
	v_exp_f32_e32 v25, v25
	v_pk_mul_f32 v[32:33], v[112:113], v[182:183]
	v_pk_mul_f32 v[96:97], v[100:101], v[102:103]
	v_pk_add_f32 v[30:31], v[30:31], 1.0 op_sel_hi:[1,0]
	v_pk_add_f32 v[24:25], v[24:25], 1.0 op_sel_hi:[1,0]
	v_rcp_f32_e32 v30, v30
	v_rcp_f32_e32 v31, v31
	v_rcp_f32_e32 v24, v24
	v_rcp_f32_e32 v25, v25
	v_pk_mul_f32 v[48:49], v[98:99], v[104:105]
	v_pk_mul_f32 v[32:33], v[32:33], v[30:31]
	v_pk_mul_f32 v[30:31], v[100:101], s[14:15] op_sel_hi:[1,0]
	v_pk_mul_f32 v[24:25], v[46:47], v[24:25]
	v_exp_f32_e32 v30, v30
	v_exp_f32_e32 v31, v31
	v_pk_mul_f32 v[46:47], v[98:99], s[14:15] op_sel_hi:[1,0]
	v_pk_mul_f32 v[56:57], v[56:57], v[166:167] op_sel_hi:[1,0]
	v_exp_f32_e32 v46, v46
	v_exp_f32_e32 v47, v47
	v_pk_add_f32 v[30:31], v[30:31], 1.0 op_sel_hi:[1,0]
	v_pk_mul_f32 v[50:51], v[50:51], v[166:167] op_sel_hi:[1,0]
	v_rcp_f32_e32 v30, v30
	v_rcp_f32_e32 v31, v31
	v_pk_add_f32 v[46:47], v[46:47], 1.0 op_sel_hi:[1,0]
	v_pk_mul_f32 v[8:9], v[8:9], v[154:155] op_sel_hi:[1,0]
	v_rcp_f32_e32 v46, v46
	v_rcp_f32_e32 v47, v47
	v_pk_mul_f32 v[96:97], v[96:97], v[30:31]
	v_cvt_pk_bf16_f32 v30, v24, v25
	v_or_b32_e32 v24, 32, v153
	v_mad_i64_i32 v[24:25], s[26:27], v24, s49, v[18:19]
	v_cvt_pk_bf16_f32 v31, v32, v33
	v_lshl_add_u64 v[24:25], v[24:25], 0, v[22:23]
	v_pk_mul_f32 v[46:47], v[48:49], v[46:47]
	v_cvt_pk_bf16_f32 v32, v96, v97
	v_pk_mul_f32 v[48:49], v[80:81], v[86:87]
	v_cvt_pk_bf16_f32 v33, v46, v47
	global_store_dwordx4 v[24:25], v[30:33], off
	v_pk_mul_f32 v[24:25], v[92:93], s[14:15] op_sel_hi:[1,0]
	v_pk_mul_f32 v[46:47], v[92:93], v[88:89]
	v_pk_mul_f32 v[30:31], v[90:91], s[14:15] op_sel_hi:[1,0]
	v_exp_f32_e32 v24, v24
	v_exp_f32_e32 v30, v30
	v_exp_f32_e32 v31, v31
	v_exp_f32_e32 v25, v25
	v_pk_mul_f32 v[32:33], v[90:91], v[94:95]
	v_pk_mul_f32 v[8:9], v[14:15], v[8:9]
	v_pk_add_f32 v[30:31], v[30:31], 1.0 op_sel_hi:[1,0]
	v_pk_add_f32 v[24:25], v[24:25], 1.0 op_sel_hi:[1,0]
	v_rcp_f32_e32 v30, v30
	v_rcp_f32_e32 v31, v31
	v_rcp_f32_e32 v24, v24
	v_rcp_f32_e32 v25, v25
	v_pk_mul_f32 v[6:7], v[6:7], v[154:155] op_sel_hi:[1,0]
	v_pk_mul_f32 v[32:33], v[32:33], v[30:31]
	v_pk_mul_f32 v[30:31], v[82:83], s[14:15] op_sel_hi:[1,0]
	v_pk_mul_f32 v[24:25], v[46:47], v[24:25]
	v_exp_f32_e32 v30, v30
	v_exp_f32_e32 v31, v31
	v_pk_mul_f32 v[46:47], v[80:81], s[14:15] op_sel_hi:[1,0]
	v_pk_mul_f32 v[80:81], v[82:83], v[84:85]
	v_exp_f32_e32 v46, v46
	v_exp_f32_e32 v47, v47
	v_pk_add_f32 v[30:31], v[30:31], 1.0 op_sel_hi:[1,0]
	v_pk_mul_f32 v[6:7], v[16:17], v[6:7]
	v_rcp_f32_e32 v30, v30
	v_rcp_f32_e32 v31, v31
	v_pk_add_f32 v[46:47], v[46:47], 1.0 op_sel_hi:[1,0]
	v_pk_mul_f32 v[2:3], v[2:3], v[154:155] op_sel_hi:[1,0]
	v_rcp_f32_e32 v46, v46
	v_rcp_f32_e32 v47, v47
	v_pk_mul_f32 v[80:81], v[80:81], v[30:31]
	v_cvt_pk_bf16_f32 v30, v24, v25
	v_or_b32_e32 v24, 48, v153
	v_mad_i64_i32 v[24:25], s[26:27], v24, s49, v[18:19]
	v_cvt_pk_bf16_f32 v31, v32, v33
	v_lshl_add_u64 v[24:25], v[24:25], 0, v[22:23]
	v_pk_mul_f32 v[46:47], v[48:49], v[46:47]
	v_cvt_pk_bf16_f32 v32, v80, v81
	v_add_u32_e32 v80, 0x80, v153
	v_cvt_pk_bf16_f32 v33, v46, v47
	global_store_dwordx4 v[24:25], v[30:33], off
	v_pk_mul_f32 v[24:25], v[74:75], s[14:15] op_sel_hi:[1,0]
	v_pk_mul_f32 v[46:47], v[74:75], v[76:77]
	v_pk_mul_f32 v[30:31], v[72:73], s[14:15] op_sel_hi:[1,0]
	v_exp_f32_e32 v24, v24
	v_exp_f32_e32 v30, v30
	v_exp_f32_e32 v31, v31
	v_exp_f32_e32 v25, v25
	v_pk_mul_f32 v[32:33], v[72:73], v[78:79]
	v_pk_mul_f32 v[48:49], v[64:65], v[70:71]
	v_pk_add_f32 v[30:31], v[30:31], 1.0 op_sel_hi:[1,0]
	v_pk_add_f32 v[24:25], v[24:25], 1.0 op_sel_hi:[1,0]
	v_rcp_f32_e32 v30, v30
	v_rcp_f32_e32 v31, v31
	v_rcp_f32_e32 v24, v24
	v_rcp_f32_e32 v25, v25
	v_pk_mul_f32 v[4:5], v[4:5], v[154:155] op_sel_hi:[1,0]
	v_pk_mul_f32 v[32:33], v[32:33], v[30:31]
	v_pk_mul_f32 v[30:31], v[66:67], s[14:15] op_sel_hi:[1,0]
	v_pk_mul_f32 v[24:25], v[46:47], v[24:25]
	v_exp_f32_e32 v30, v30
	v_exp_f32_e32 v31, v31
	v_pk_mul_f32 v[46:47], v[64:65], s[14:15] op_sel_hi:[1,0]
	v_pk_mul_f32 v[64:65], v[66:67], v[68:69]
	v_exp_f32_e32 v46, v46
	v_exp_f32_e32 v47, v47
	v_pk_add_f32 v[30:31], v[30:31], 1.0 op_sel_hi:[1,0]
	v_pk_mul_f32 v[2:3], v[12:13], v[2:3]
	v_rcp_f32_e32 v30, v30
	v_rcp_f32_e32 v31, v31
	v_pk_add_f32 v[46:47], v[46:47], 1.0 op_sel_hi:[1,0]
	v_pk_mul_f32 v[4:5], v[10:11], v[4:5]
	v_rcp_f32_e32 v46, v46
	v_rcp_f32_e32 v47, v47
	v_pk_mul_f32 v[64:65], v[64:65], v[30:31]
	v_cvt_pk_bf16_f32 v30, v24, v25
	v_mad_i64_i32 v[24:25], s[26:27], v80, s49, v[18:19]
	v_cvt_pk_bf16_f32 v31, v32, v33
	v_lshl_add_u64 v[24:25], v[24:25], 0, v[22:23]
	v_pk_mul_f32 v[46:47], v[48:49], v[46:47]
	v_cvt_pk_bf16_f32 v32, v64, v65
	v_pk_mul_f32 v[48:49], v[50:51], v[52:53]
	v_cvt_pk_bf16_f32 v33, v46, v47
	global_store_dwordx4 v[24:25], v[30:33], off
	v_pk_mul_f32 v[24:25], v[58:59], s[14:15] op_sel_hi:[1,0]
	v_pk_mul_f32 v[46:47], v[58:59], v[60:61]
	v_pk_mul_f32 v[30:31], v[56:57], s[14:15] op_sel_hi:[1,0]
	v_exp_f32_e32 v24, v24
	v_exp_f32_e32 v30, v30
	v_exp_f32_e32 v31, v31
	v_exp_f32_e32 v25, v25
	v_pk_mul_f32 v[32:33], v[56:57], v[62:63]
	v_pk_add_f32 v[30:31], v[30:31], 1.0 op_sel_hi:[1,0]
	s_nop 0
	v_rcp_f32_e32 v30, v30
	v_rcp_f32_e32 v31, v31
	v_pk_add_f32 v[24:25], v[24:25], 1.0 op_sel_hi:[1,0]
	v_pk_mul_f32 v[32:33], v[32:33], v[30:31]
	v_rcp_f32_e32 v24, v24
	v_rcp_f32_e32 v25, v25
	v_pk_mul_f32 v[30:31], v[50:51], s[14:15] op_sel_hi:[1,0]
	v_pk_mul_f32 v[24:25], v[46:47], v[24:25]
	v_exp_f32_e32 v30, v30
	v_exp_f32_e32 v31, v31
	v_pk_mul_f32 v[46:47], v[44:45], s[14:15] op_sel_hi:[1,0]
	v_pk_mul_f32 v[44:45], v[44:45], v[54:55]
	v_exp_f32_e32 v46, v46
	v_exp_f32_e32 v47, v47
	v_pk_add_f32 v[30:31], v[30:31], 1.0 op_sel_hi:[1,0]
	v_pk_add_f32 v[46:47], v[46:47], 1.0 op_sel_hi:[1,0]
	v_rcp_f32_e32 v30, v30
	v_rcp_f32_e32 v31, v31
	v_rcp_f32_e32 v46, v46
	v_rcp_f32_e32 v47, v47
	v_pk_mul_f32 v[48:49], v[48:49], v[30:31]
	v_cvt_pk_bf16_f32 v30, v24, v25
	v_add_u32_e32 v24, 0x90, v153
	v_mad_i64_i32 v[24:25], s[26:27], v24, s49, v[18:19]
	v_cvt_pk_bf16_f32 v31, v32, v33
	v_lshl_add_u64 v[24:25], v[24:25], 0, v[22:23]
	v_pk_mul_f32 v[44:45], v[44:45], v[46:47]
	v_cvt_pk_bf16_f32 v32, v48, v49
	s_nop 0
	v_cvt_pk_bf16_f32 v33, v44, v45
	global_store_dwordx4 v[24:25], v[30:33], off
	v_pk_mul_f32 v[24:25], v[42:43], s[14:15] op_sel_hi:[1,0]
	s_nop 0
	v_pk_mul_f32 v[30:31], v[36:37], s[14:15] op_sel_hi:[1,0]
	v_exp_f32_e32 v24, v24
	v_exp_f32_e32 v25, v25
	v_exp_f32_e32 v30, v30
	v_exp_f32_e32 v31, v31
	v_pk_mul_f32 v[32:33], v[36:37], v[40:41]
	v_pk_add_f32 v[24:25], v[24:25], 1.0 op_sel_hi:[1,0]
	v_pk_mul_f32 v[36:37], v[42:43], v[38:39]
	v_pk_add_f32 v[30:31], v[30:31], 1.0 op_sel_hi:[1,0]
	v_rcp_f32_e32 v24, v24
	v_rcp_f32_e32 v25, v25
	v_rcp_f32_e32 v30, v30
	v_rcp_f32_e32 v31, v31
	v_pk_mul_f32 v[24:25], v[36:37], v[24:25]
	v_pk_mul_f32 v[36:37], v[20:21], s[14:15] op_sel_hi:[1,0]
	v_pk_mul_f32 v[30:31], v[32:33], v[30:31]
	v_pk_mul_f32 v[32:33], v[26:27], s[14:15] op_sel_hi:[1,0]
	v_exp_f32_e32 v36, v36
	v_exp_f32_e32 v32, v32
	v_exp_f32_e32 v33, v33
	v_exp_f32_e32 v37, v37
	v_pk_mul_f32 v[20:21], v[20:21], v[34:35]
	v_pk_mul_f32 v[26:27], v[26:27], v[28:29]
	v_pk_add_f32 v[32:33], v[32:33], 1.0 op_sel_hi:[1,0]
	v_pk_add_f32 v[36:37], v[36:37], 1.0 op_sel_hi:[1,0]
	v_rcp_f32_e32 v32, v32
	v_rcp_f32_e32 v33, v33
	v_rcp_f32_e32 v36, v36
	v_rcp_f32_e32 v37, v37
	v_cvt_pk_bf16_f32 v24, v24, v25
	v_pk_mul_f32 v[26:27], v[26:27], v[32:33]
	v_cvt_pk_bf16_f32 v25, v30, v31
	v_pk_mul_f32 v[20:21], v[20:21], v[36:37]
	v_cvt_pk_bf16_f32 v26, v26, v27
	s_nop 0
	v_cvt_pk_bf16_f32 v27, v20, v21
	v_add_u32_e32 v20, 0xa0, v153
	v_mad_i64_i32 v[20:21], s[26:27], v20, s49, v[18:19]
	v_lshl_add_u64 v[20:21], v[20:21], 0, v[22:23]
	global_store_dwordx4 v[20:21], v[24:27], off
	v_pk_mul_f32 v[20:21], v[16:17], s[14:15] op_sel_hi:[1,0]
	v_pk_mul_f32 v[16:17], v[10:11], s[14:15] op_sel_hi:[1,0]
	v_exp_f32_e32 v20, v20
	v_exp_f32_e32 v21, v21
	v_pk_mul_f32 v[24:25], v[14:15], s[14:15] op_sel_hi:[1,0]
	v_pk_mul_f32 v[14:15], v[12:13], s[14:15] op_sel_hi:[1,0]
	v_exp_f32_e32 v24, v24
	v_exp_f32_e32 v14, v14
	v_exp_f32_e32 v15, v15
	v_exp_f32_e32 v25, v25
	v_pk_add_f32 v[20:21], v[20:21], 1.0 op_sel_hi:[1,0]
	v_exp_f32_e32 v16, v16
	v_exp_f32_e32 v17, v17
	v_rcp_f32_e32 v20, v20
	v_rcp_f32_e32 v21, v21
	v_pk_add_f32 v[14:15], v[14:15], 1.0 op_sel_hi:[1,0]
	v_pk_add_f32 v[24:25], v[24:25], 1.0 op_sel_hi:[1,0]
	v_rcp_f32_e32 v14, v14
	v_rcp_f32_e32 v15, v15
	v_pk_add_f32 v[16:17], v[16:17], 1.0 op_sel_hi:[1,0]
	v_rcp_f32_e32 v24, v24
	v_rcp_f32_e32 v25, v25
	v_pk_mul_f32 v[6:7], v[6:7], v[20:21]
	v_rcp_f32_e32 v16, v16
	v_rcp_f32_e32 v17, v17
	v_pk_mul_f32 v[10:11], v[2:3], v[14:15]
	v_cvt_pk_bf16_f32 v2, v6, v7
	v_add_u32_e32 v6, 0xb0, v153
	v_mad_i64_i32 v[6:7], s[26:27], v6, s49, v[18:19]
	v_lshl_add_u64 v[6:7], v[6:7], 0, v[22:23]
	v_pk_mul_f32 v[8:9], v[8:9], v[24:25]
	v_pk_mul_f32 v[12:13], v[4:5], v[16:17]
	v_cvt_pk_bf16_f32 v3, v8, v9
	v_cvt_pk_bf16_f32 v4, v10, v11
	s_nop 0
	v_cvt_pk_bf16_f32 v5, v12, v13
	global_store_dwordx4 v[6:7], v[2:5], off
	s_cbranch_vccnz .LBB0_1475
	s_andn2_b64 vcc, exec, s[4:5]
	s_cbranch_vccnz .LBB0_1474
	s_barrier
	s_branch .LBB0_1474

.LBB0_1696:
	s_ashr_i32 s37, s36, 31
	s_lshl_b64 s[38:39], s[36:37], 20
	s_add_u32 s38, s20, s38
	s_addc_u32 s39, s21, s39
	s_and_b64 s[40:41], s[10:11], exec
	s_cselect_b32 s37, s39, s47
	s_cselect_b32 s43, s38, s46
	s_ashr_i32 s35, s34, 31
	s_lshl_b64 s[40:41], s[34:35], 20
	s_add_u32 s40, s23, s40
	s_addc_u32 s41, s33, s41
	s_and_b64 s[50:51], s[10:11], exec
	s_cselect_b32 s35, s41, s49
	s_cselect_b32 s45, s40, s48
	s_lshl_b32 s50, s44, 8
	s_ashr_i32 s51, s50, 31
	v_lshl_add_u64 v[238:239], s[50:51], 2, v[140:141]
	global_load_dword v240, v[238:239], off
	global_load_dword v242, v[238:239], off offset:64
	global_load_dword v244, v[238:239], off offset:128
	global_load_dword v246, v[238:239], off offset:192
	global_load_dword v248, v[238:239], off offset:512
	global_load_dword v250, v[238:239], off offset:576
	global_load_dword v252, v[238:239], off offset:640
	global_load_dword v238, v[238:239], off offset:704
	s_add_u32 s46, s46, 0x80080
	s_addc_u32 s47, s47, 0
	s_add_u32 s69, s48, 0x100
	s_addc_u32 s70, s49, 0
	s_mov_b32 s71, -2
	s_waitcnt vmcnt(0)
	ds_read_b128 v[156:159], v176
	ds_read_b128 v[160:163], v176 offset:1024
	ds_read_b128 v[164:167], v176 offset:2048
	ds_read_b128 v[168:171], v176 offset:3072
	ds_read_b128 v[180:183], v177
	ds_read_b128 v[184:187], v177 offset:1024
	ds_read_b128 v[188:191], v177 offset:2048
	ds_read_b128 v[192:195], v177 offset:3072
	s_add_u32 s48, s46, 0xfff80080
	s_addc_u32 s49, s47, -1
	s_cmp_eq_u32 s71, 28
	s_cselect_b32 s51, s37, s49
	s_cselect_b32 s50, s43, s48
	s_cselect_b32 s49, s35, s70
	s_cselect_b32 s48, s45, s69
	v_lshl_add_u64 v[172:173], s[46:47], 0, v[148:149]
	s_add_i32 m0, s53, 0xc000
	ds_read_b128 v[196:199], v178
	ds_read_b128 v[200:203], v178 offset:1024
	ds_read_b128 v[204:207], v178 offset:2048
	ds_read_b128 v[208:211], v178 offset:3072
	ds_read_b128 v[212:215], v178 offset:4096
	ds_read_b128 v[216:219], v178 offset:5120
	ds_read_b128 v[220:223], v178 offset:6144
	ds_read_b128 v[224:227], v178 offset:7168
	global_load_lds_dwordx4 v[172:173], off
	v_lshl_add_u64 v[172:173], s[46:47], 0, v[150:151]
	s_add_i32 m0, s53, 0xe000
	s_nop 0
	global_load_lds_dwordx4 v[172:173], off
	s_waitcnt vmcnt(8)
	s_waitcnt lgkmcnt(0)
	s_setprio 1
	s_barrier
	v_mfma_f32_16x16x32_bf16 v[126:129], v[156:159], v[196:199], 0
	v_mfma_f32_16x16x32_bf16 v[122:125], v[164:167], v[196:199], 0
	v_mfma_f32_16x16x32_bf16 v[118:121], v[156:159], v[204:207], 0
	v_mfma_f32_16x16x32_bf16 v[114:117], v[164:167], v[204:207], 0
	v_mfma_f32_16x16x32_bf16 v[110:113], v[156:159], v[212:215], 0
	v_mfma_f32_16x16x32_bf16 v[106:109], v[164:167], v[212:215], 0
	v_mfma_f32_16x16x32_bf16 v[102:105], v[156:159], v[220:223], 0
	v_mfma_f32_16x16x32_bf16 v[98:101], v[164:167], v[220:223], 0
	v_mfma_f32_16x16x32_bf16 v[126:129], v[160:163], v[200:203], v[126:129]
	v_mfma_f32_16x16x32_bf16 v[122:125], v[168:171], v[200:203], v[122:125]
	v_mfma_f32_16x16x32_bf16 v[118:121], v[160:163], v[208:211], v[118:121]
	v_mfma_f32_16x16x32_bf16 v[114:117], v[168:171], v[208:211], v[114:117]
	v_mfma_f32_16x16x32_bf16 v[110:113], v[160:163], v[216:219], v[110:113]
	v_mfma_f32_16x16x32_bf16 v[106:109], v[168:171], v[216:219], v[106:109]
	v_mfma_f32_16x16x32_bf16 v[102:105], v[160:163], v[224:227], v[102:105]
	v_mfma_f32_16x16x32_bf16 v[98:101], v[168:171], v[224:227], v[98:101]
	s_setprio 0
	s_setprio 1
	v_mfma_f32_16x16x32_bf16 v[38:41], v[180:183], v[196:199], 0
	v_mfma_f32_16x16x32_bf16 v[34:37], v[188:191], v[196:199], 0
	v_mfma_f32_16x16x32_bf16 v[46:49], v[180:183], v[204:207], 0
	v_mfma_f32_16x16x32_bf16 v[42:45], v[188:191], v[204:207], 0
	v_mfma_f32_16x16x32_bf16 v[54:57], v[180:183], v[212:215], 0
	v_mfma_f32_16x16x32_bf16 v[50:53], v[188:191], v[212:215], 0
	v_mfma_f32_16x16x32_bf16 v[62:65], v[180:183], v[220:223], 0
	v_mfma_f32_16x16x32_bf16 v[58:61], v[188:191], v[220:223], 0
	v_mfma_f32_16x16x32_bf16 v[38:41], v[184:187], v[200:203], v[38:41]
	v_mfma_f32_16x16x32_bf16 v[34:37], v[192:195], v[200:203], v[34:37]
	v_mfma_f32_16x16x32_bf16 v[46:49], v[184:187], v[208:211], v[46:49]
	v_mfma_f32_16x16x32_bf16 v[42:45], v[192:195], v[208:211], v[42:45]
	v_mfma_f32_16x16x32_bf16 v[54:57], v[184:187], v[216:219], v[54:57]
	v_mfma_f32_16x16x32_bf16 v[50:53], v[192:195], v[216:219], v[50:53]
	v_mfma_f32_16x16x32_bf16 v[62:65], v[184:187], v[224:227], v[62:65]
	v_mfma_f32_16x16x32_bf16 v[58:61], v[192:195], v[224:227], v[58:61]
	s_barrier
	s_setprio 0
	s_add_i32 s72, s65, s52
	v_lshl_add_u64 v[172:173], s[48:49], 0, v[132:133]
	s_mov_b32 m0, s72
	ds_read_b128 v[196:199], v178 offset:16384
	ds_read_b128 v[200:203], v178 offset:17408
	ds_read_b128 v[204:207], v178 offset:18432
	ds_read_b128 v[208:211], v178 offset:19456
	ds_read_b128 v[212:215], v178 offset:20480
	ds_read_b128 v[216:219], v178 offset:21504
	ds_read_b128 v[220:223], v178 offset:22528
	ds_read_b128 v[224:227], v178 offset:23552
	global_load_lds_dwordx4 v[172:173], off
	s_add_i32 m0, s72, 0x2000
	s_add_u32 s72, s48, 0x80000
	v_lshl_add_u64 v[228:229], s[48:49], 0, v[136:137]
	s_addc_u32 s73, s49, 0
	s_add_i32 s74, s66, s52
	global_load_lds_dwordx4 v[228:229], off
	v_lshl_add_u64 v[230:231], s[72:73], 0, v[132:133]
	s_mov_b32 m0, s74
	v_lshl_add_u64 v[232:233], s[50:51], 0, v[134:135]
	global_load_lds_dwordx4 v[230:231], off
	v_lshl_add_u64 v[230:231], s[72:73], 0, v[136:137]
	s_add_i32 m0, s74, 0x2000
	s_nop 0
	global_load_lds_dwordx4 v[230:231], off
	v_lshl_add_u64 v[230:231], s[50:51], 0, v[130:131]
	s_mov_b32 m0, s53
	s_nop 0
	global_load_lds_dwordx4 v[230:231], off
	s_mov_b32 m0, s54
	s_nop 0
	global_load_lds_dwordx4 v[232:233], off
	s_waitcnt vmcnt(8)
	s_waitcnt lgkmcnt(0)
	s_setprio 1
	s_barrier
	v_mfma_f32_16x16x32_bf16 v[94:97], v[156:159], v[196:199], 0
	v_mfma_f32_16x16x32_bf16 v[90:93], v[164:167], v[196:199], 0
	v_mfma_f32_16x16x32_bf16 v[86:89], v[156:159], v[204:207], 0
	v_mfma_f32_16x16x32_bf16 v[82:85], v[164:167], v[204:207], 0
	v_mfma_f32_16x16x32_bf16 v[78:81], v[156:159], v[212:215], 0
	v_mfma_f32_16x16x32_bf16 v[74:77], v[164:167], v[212:215], 0
	v_mfma_f32_16x16x32_bf16 v[70:73], v[156:159], v[220:223], 0
	v_mfma_f32_16x16x32_bf16 v[66:69], v[164:167], v[220:223], 0
	v_mfma_f32_16x16x32_bf16 v[94:97], v[160:163], v[200:203], v[94:97]
	v_mfma_f32_16x16x32_bf16 v[90:93], v[168:171], v[200:203], v[90:93]
	v_mfma_f32_16x16x32_bf16 v[86:89], v[160:163], v[208:211], v[86:89]
	v_mfma_f32_16x16x32_bf16 v[82:85], v[168:171], v[208:211], v[82:85]
	v_mfma_f32_16x16x32_bf16 v[78:81], v[160:163], v[216:219], v[78:81]
	v_mfma_f32_16x16x32_bf16 v[74:77], v[168:171], v[216:219], v[74:77]
	v_mfma_f32_16x16x32_bf16 v[70:73], v[160:163], v[224:227], v[70:73]
	v_mfma_f32_16x16x32_bf16 v[66:69], v[168:171], v[224:227], v[66:69]
	s_setprio 0
	s_setprio 1
	v_mfma_f32_16x16x32_bf16 v[6:9], v[180:183], v[196:199], 0
	v_mfma_f32_16x16x32_bf16 v[2:5], v[188:191], v[196:199], 0
	v_mfma_f32_16x16x32_bf16 v[18:21], v[180:183], v[204:207], 0
	v_mfma_f32_16x16x32_bf16 v[14:17], v[188:191], v[204:207], 0
	v_mfma_f32_16x16x32_bf16 v[26:29], v[180:183], v[212:215], 0
	v_mfma_f32_16x16x32_bf16 v[22:25], v[188:191], v[212:215], 0
	v_mfma_f32_16x16x32_bf16 v[30:33], v[180:183], v[220:223], 0
	v_mfma_f32_16x16x32_bf16 v[10:13], v[188:191], v[220:223], 0
	v_mfma_f32_16x16x32_bf16 v[6:9], v[184:187], v[200:203], v[6:9]
	v_mfma_f32_16x16x32_bf16 v[2:5], v[192:195], v[200:203], v[2:5]
	v_mfma_f32_16x16x32_bf16 v[18:21], v[184:187], v[208:211], v[18:21]
	v_mfma_f32_16x16x32_bf16 v[14:17], v[192:195], v[208:211], v[14:17]
	v_mfma_f32_16x16x32_bf16 v[26:29], v[184:187], v[216:219], v[26:29]
	v_mfma_f32_16x16x32_bf16 v[22:25], v[192:195], v[216:219], v[22:25]
	v_mfma_f32_16x16x32_bf16 v[30:33], v[184:187], v[224:227], v[30:33]
	v_mfma_f32_16x16x32_bf16 v[10:13], v[192:195], v[224:227], v[10:13]
	s_barrier
	s_setprio 0
	s_add_i32 s72, 0, 0x18000
	v_add_u32_e32 v138, s72, v174
	s_add_i32 s73, 0, 0x1c000
	ds_read_b128 v[156:159], v138
	ds_read_b128 v[160:163], v138 offset:1024
	ds_read_b128 v[164:167], v138 offset:2048
	ds_read_b128 v[168:171], v138 offset:3072
	v_add_u32_e32 v138, s73, v174
	ds_read_b128 v[180:183], v138
	ds_read_b128 v[184:187], v138 offset:1024
	ds_read_b128 v[188:191], v138 offset:2048
	ds_read_b128 v[192:195], v138 offset:3072
	s_add_u32 s50, s50, 0x80000
	s_addc_u32 s51, s51, 0
	s_mov_b32 m0, s55
	v_lshl_add_u64 v[234:235], s[50:51], 0, v[130:131]
	ds_read_b128 v[196:199], v178 offset:32768
	ds_read_b128 v[200:203], v178 offset:33792
	ds_read_b128 v[204:207], v178 offset:34816
	ds_read_b128 v[208:211], v178 offset:35840
	ds_read_b128 v[212:215], v178 offset:36864
	ds_read_b128 v[216:219], v178 offset:37888
	ds_read_b128 v[220:223], v178 offset:38912
	ds_read_b128 v[224:227], v178 offset:39936
	global_load_lds_dwordx4 v[234:235], off
	v_lshl_add_u64 v[234:235], s[50:51], 0, v[134:135]
	s_mov_b32 m0, s56
	s_nop 0
	global_load_lds_dwordx4 v[234:235], off
	s_waitcnt vmcnt(8)
	s_waitcnt lgkmcnt(0)
	s_setprio 1
	s_barrier
	v_mfma_f32_16x16x32_bf16 v[126:129], v[156:159], v[196:199], v[126:129]
	v_mfma_f32_16x16x32_bf16 v[122:125], v[164:167], v[196:199], v[122:125]
	v_mfma_f32_16x16x32_bf16 v[118:121], v[156:159], v[204:207], v[118:121]
	v_mfma_f32_16x16x32_bf16 v[114:117], v[164:167], v[204:207], v[114:117]
	v_mfma_f32_16x16x32_bf16 v[110:113], v[156:159], v[212:215], v[110:113]
	v_mfma_f32_16x16x32_bf16 v[106:109], v[164:167], v[212:215], v[106:109]
	v_mfma_f32_16x16x32_bf16 v[102:105], v[156:159], v[220:223], v[102:105]
	v_mfma_f32_16x16x32_bf16 v[98:101], v[164:167], v[220:223], v[98:101]
	v_mfma_f32_16x16x32_bf16 v[126:129], v[160:163], v[200:203], v[126:129]
	v_mfma_f32_16x16x32_bf16 v[122:125], v[168:171], v[200:203], v[122:125]
	v_mfma_f32_16x16x32_bf16 v[118:121], v[160:163], v[208:211], v[118:121]
	v_mfma_f32_16x16x32_bf16 v[114:117], v[168:171], v[208:211], v[114:117]
	v_mfma_f32_16x16x32_bf16 v[110:113], v[160:163], v[216:219], v[110:113]
	v_mfma_f32_16x16x32_bf16 v[106:109], v[168:171], v[216:219], v[106:109]
	v_mfma_f32_16x16x32_bf16 v[102:105], v[160:163], v[224:227], v[102:105]
	v_mfma_f32_16x16x32_bf16 v[98:101], v[168:171], v[224:227], v[98:101]
	s_setprio 0
	s_setprio 1
	v_mfma_f32_16x16x32_bf16 v[38:41], v[180:183], v[196:199], v[38:41]
	v_mfma_f32_16x16x32_bf16 v[34:37], v[188:191], v[196:199], v[34:37]
	v_mfma_f32_16x16x32_bf16 v[46:49], v[180:183], v[204:207], v[46:49]
	v_mfma_f32_16x16x32_bf16 v[42:45], v[188:191], v[204:207], v[42:45]
	v_mfma_f32_16x16x32_bf16 v[54:57], v[180:183], v[212:215], v[54:57]
	v_mfma_f32_16x16x32_bf16 v[50:53], v[188:191], v[212:215], v[50:53]
	v_mfma_f32_16x16x32_bf16 v[62:65], v[180:183], v[220:223], v[62:65]
	v_mfma_f32_16x16x32_bf16 v[58:61], v[188:191], v[220:223], v[58:61]
	v_mfma_f32_16x16x32_bf16 v[38:41], v[184:187], v[200:203], v[38:41]
	v_mfma_f32_16x16x32_bf16 v[34:37], v[192:195], v[200:203], v[34:37]
	v_mfma_f32_16x16x32_bf16 v[46:49], v[184:187], v[208:211], v[46:49]
	v_mfma_f32_16x16x32_bf16 v[42:45], v[192:195], v[208:211], v[42:45]
	v_mfma_f32_16x16x32_bf16 v[54:57], v[184:187], v[216:219], v[54:57]
	v_mfma_f32_16x16x32_bf16 v[50:53], v[192:195], v[216:219], v[50:53]
	v_mfma_f32_16x16x32_bf16 v[62:65], v[184:187], v[224:227], v[62:65]
	v_mfma_f32_16x16x32_bf16 v[58:61], v[192:195], v[224:227], v[58:61]
	s_barrier
	s_setprio 0
	s_add_i32 s50, s72, s52
	v_lshl_add_u64 v[172:173], v[172:173], 0, s[6:7]
	s_mov_b32 m0, s50
	ds_read_b128 v[196:199], v178 offset:49152
	ds_read_b128 v[200:203], v178 offset:50176
	ds_read_b128 v[204:207], v178 offset:51200
	ds_read_b128 v[208:211], v178 offset:52224
	ds_read_b128 v[212:215], v178 offset:53248
	ds_read_b128 v[216:219], v178 offset:54272
	ds_read_b128 v[220:223], v178 offset:55296
	ds_read_b128 v[224:227], v178 offset:56320
	global_load_lds_dwordx4 v[172:173], off
	s_add_i32 m0, s50, 0x2000
	s_add_u32 s48, s48, 0x80080
	v_lshl_add_u64 v[172:173], v[228:229], 0, s[6:7]
	s_addc_u32 s49, s49, 0
	s_add_i32 s50, s73, s52
	global_load_lds_dwordx4 v[172:173], off
	v_lshl_add_u64 v[172:173], s[48:49], 0, v[132:133]
	s_mov_b32 m0, s50
	s_nop 0
	global_load_lds_dwordx4 v[172:173], off
	v_lshl_add_u64 v[172:173], s[48:49], 0, v[136:137]
	s_add_i32 m0, s50, 0x2000
	s_nop 0
	global_load_lds_dwordx4 v[172:173], off
	v_lshl_add_u64 v[172:173], v[230:231], 0, s[6:7]
	s_mov_b32 m0, s61
	s_nop 0
	global_load_lds_dwordx4 v[172:173], off
	v_lshl_add_u64 v[172:173], v[232:233], 0, s[6:7]
	s_mov_b32 m0, s62
	s_nop 0
	global_load_lds_dwordx4 v[172:173], off
	s_waitcnt vmcnt(8)
	s_waitcnt lgkmcnt(0)
	s_setprio 1
	s_barrier
	v_mfma_f32_16x16x32_bf16 v[94:97], v[156:159], v[196:199], v[94:97]
	v_mfma_f32_16x16x32_bf16 v[90:93], v[164:167], v[196:199], v[90:93]
	v_mfma_f32_16x16x32_bf16 v[86:89], v[156:159], v[204:207], v[86:89]
	v_mfma_f32_16x16x32_bf16 v[82:85], v[164:167], v[204:207], v[82:85]
	v_mfma_f32_16x16x32_bf16 v[78:81], v[156:159], v[212:215], v[78:81]
	v_mfma_f32_16x16x32_bf16 v[74:77], v[164:167], v[212:215], v[74:77]
	v_mfma_f32_16x16x32_bf16 v[70:73], v[156:159], v[220:223], v[70:73]
	v_mfma_f32_16x16x32_bf16 v[66:69], v[164:167], v[220:223], v[66:69]
	v_mfma_f32_16x16x32_bf16 v[94:97], v[160:163], v[200:203], v[94:97]
	v_mfma_f32_16x16x32_bf16 v[90:93], v[168:171], v[200:203], v[90:93]
	v_mfma_f32_16x16x32_bf16 v[86:89], v[160:163], v[208:211], v[86:89]
	v_mfma_f32_16x16x32_bf16 v[82:85], v[168:171], v[208:211], v[82:85]
	v_mfma_f32_16x16x32_bf16 v[78:81], v[160:163], v[216:219], v[78:81]
	v_mfma_f32_16x16x32_bf16 v[74:77], v[168:171], v[216:219], v[74:77]
	v_mfma_f32_16x16x32_bf16 v[70:73], v[160:163], v[224:227], v[70:73]
	v_mfma_f32_16x16x32_bf16 v[66:69], v[168:171], v[224:227], v[66:69]
	s_setprio 0
	s_setprio 1
	v_mfma_f32_16x16x32_bf16 v[6:9], v[180:183], v[196:199], v[6:9]
	v_mfma_f32_16x16x32_bf16 v[2:5], v[188:191], v[196:199], v[2:5]
	v_mfma_f32_16x16x32_bf16 v[18:21], v[180:183], v[204:207], v[18:21]
	v_mfma_f32_16x16x32_bf16 v[14:17], v[188:191], v[204:207], v[14:17]
	v_mfma_f32_16x16x32_bf16 v[26:29], v[180:183], v[212:215], v[26:29]
	v_mfma_f32_16x16x32_bf16 v[22:25], v[188:191], v[212:215], v[22:25]
	v_mfma_f32_16x16x32_bf16 v[30:33], v[180:183], v[220:223], v[30:33]
	v_mfma_f32_16x16x32_bf16 v[10:13], v[188:191], v[220:223], v[10:13]
	v_mfma_f32_16x16x32_bf16 v[6:9], v[184:187], v[200:203], v[6:9]
	v_mfma_f32_16x16x32_bf16 v[2:5], v[192:195], v[200:203], v[2:5]
	v_mfma_f32_16x16x32_bf16 v[18:21], v[184:187], v[208:211], v[18:21]
	v_mfma_f32_16x16x32_bf16 v[14:17], v[192:195], v[208:211], v[14:17]
	v_mfma_f32_16x16x32_bf16 v[26:29], v[184:187], v[216:219], v[26:29]
	v_mfma_f32_16x16x32_bf16 v[22:25], v[192:195], v[216:219], v[22:25]
	v_mfma_f32_16x16x32_bf16 v[30:33], v[184:187], v[224:227], v[30:33]
	v_mfma_f32_16x16x32_bf16 v[10:13], v[192:195], v[224:227], v[10:13]
	s_barrier
	s_setprio 0
	s_add_i32 s71, s71, 2
	s_add_u32 s46, s46, 0x100
	s_addc_u32 s47, s47, 0
	s_add_u32 s69, s69, 0x100
	s_addc_u32 s70, s70, 0
	s_cmp_gt_u32 s71, 29

.LBB0_1700:
	s_lshl_b32 s44, s44, 8
	s_ashr_i32 s45, s44, 31
	v_lshl_add_u64 v[156:157], s[44:45], 2, v[140:141]
	v_mov_b32_e32 v158, v240
	v_mov_b32_e32 v160, v242
	v_mov_b32_e32 v162, v244
	v_mov_b32_e32 v164, v246
	v_mov_b32_e32 v166, v248
	v_mov_b32_e32 v168, v250
	v_mov_b32_e32 v170, v252
	v_mov_b32_e32 v172, v238
	s_add_i32 s35, s44, s60
	v_or_b32_e32 v156, s35, v1
	s_cmp_lg_u32 s42, 24
	s_mov_b64 s[44:45], -1
	v_pk_mul_f32 v[128:129], v[128:129], v[158:159] op_sel_hi:[1,0]
	v_pk_mul_f32 v[126:127], v[126:127], v[158:159] op_sel_hi:[1,0]
	v_pk_mul_f32 v[124:125], v[124:125], v[158:159] op_sel_hi:[1,0]
	v_pk_mul_f32 v[122:123], v[122:123], v[158:159] op_sel_hi:[1,0]
	v_pk_mul_f32 v[120:121], v[120:121], v[160:161] op_sel_hi:[1,0]
	v_pk_mul_f32 v[118:119], v[118:119], v[160:161] op_sel_hi:[1,0]
	v_pk_mul_f32 v[116:117], v[116:117], v[160:161] op_sel_hi:[1,0]
	v_pk_mul_f32 v[114:115], v[114:115], v[160:161] op_sel_hi:[1,0]
	v_pk_mul_f32 v[112:113], v[112:113], v[162:163] op_sel_hi:[1,0]
	v_pk_mul_f32 v[110:111], v[110:111], v[162:163] op_sel_hi:[1,0]
	v_pk_mul_f32 v[108:109], v[108:109], v[162:163] op_sel_hi:[1,0]
	v_pk_mul_f32 v[106:107], v[106:107], v[162:163] op_sel_hi:[1,0]
	v_pk_mul_f32 v[104:105], v[104:105], v[164:165] op_sel_hi:[1,0]
	v_pk_mul_f32 v[102:103], v[102:103], v[164:165] op_sel_hi:[1,0]
	v_pk_mul_f32 v[100:101], v[100:101], v[164:165] op_sel_hi:[1,0]
	v_pk_mul_f32 v[98:99], v[98:99], v[164:165] op_sel_hi:[1,0]
	v_pk_mul_f32 v[96:97], v[96:97], v[166:167] op_sel_hi:[1,0]
	v_pk_mul_f32 v[94:95], v[94:95], v[166:167] op_sel_hi:[1,0]
	v_pk_mul_f32 v[92:93], v[92:93], v[166:167] op_sel_hi:[1,0]
	v_pk_mul_f32 v[90:91], v[90:91], v[166:167] op_sel_hi:[1,0]
	v_pk_mul_f32 v[88:89], v[88:89], v[168:169] op_sel_hi:[1,0]
	v_pk_mul_f32 v[86:87], v[86:87], v[168:169] op_sel_hi:[1,0]
	v_pk_mul_f32 v[84:85], v[84:85], v[168:169] op_sel_hi:[1,0]
	v_pk_mul_f32 v[82:83], v[82:83], v[168:169] op_sel_hi:[1,0]
	v_pk_mul_f32 v[80:81], v[80:81], v[170:171] op_sel_hi:[1,0]
	v_pk_mul_f32 v[78:79], v[78:79], v[170:171] op_sel_hi:[1,0]
	v_pk_mul_f32 v[76:77], v[76:77], v[170:171] op_sel_hi:[1,0]
	v_pk_mul_f32 v[74:75], v[74:75], v[170:171] op_sel_hi:[1,0]
	v_pk_mul_f32 v[72:73], v[72:73], v[172:173] op_sel_hi:[1,0]
	v_pk_mul_f32 v[70:71], v[70:71], v[172:173] op_sel_hi:[1,0]
	v_pk_mul_f32 v[68:69], v[68:69], v[172:173] op_sel_hi:[1,0]
	v_pk_mul_f32 v[66:67], v[66:67], v[172:173] op_sel_hi:[1,0]
	s_cbranch_scc0 .LBB0_1702
	v_mov_b32_e32 v171, v170
	v_mov_b32_e32 v173, v172
	s_ashr_i32 s44, s42, 3
	v_mov_b32_e32 v167, v166
	v_mov_b32_e32 v180, v172
	v_mov_b32_e32 v181, v172
	v_pk_mul_f32 v[10:11], v[10:11], v[172:173]
	v_pk_mul_f32 v[30:31], v[30:31], v[172:173]
	v_mov_b32_e32 v172, v170
	v_mov_b32_e32 v173, v170
	v_pk_mul_f32 v[22:23], v[22:23], v[170:171]
	v_pk_mul_f32 v[26:27], v[26:27], v[170:171]
	v_mov_b32_e32 v170, v168
	v_mov_b32_e32 v171, v168
	s_ashr_i32 s45, s44, 31
	v_pk_mul_f32 v[16:17], v[16:17], v[170:171]
	v_pk_mul_f32 v[20:21], v[20:21], v[170:171]
	v_pk_mul_f32 v[170:171], v[2:3], v[166:167]
	v_mov_b32_e32 v2, v164
	v_mov_b32_e32 v3, v164
	s_lshl_b64 s[44:45], s[44:45], 27
	v_pk_mul_f32 v[60:61], v[60:61], v[2:3]
	v_pk_mul_f32 v[64:65], v[64:65], v[2:3]
	v_mov_b32_e32 v2, v162
	v_mov_b32_e32 v3, v162
	s_add_u32 s44, s58, s44
	v_pk_mul_f32 v[52:53], v[52:53], v[2:3]
	v_pk_mul_f32 v[56:57], v[56:57], v[2:3]
	v_mov_b32_e32 v2, v160
	v_mov_b32_e32 v3, v160
	s_addc_u32 s45, s59, s45
	s_lshl_b32 s37, s42, 8
	v_pk_mul_f32 v[44:45], v[44:45], v[2:3]
	v_pk_mul_f32 v[48:49], v[48:49], v[2:3]
	v_mov_b32_e32 v2, v158
	v_mov_b32_e32 v3, v158
	s_and_b32 s37, s37, 0x700
	v_pk_mul_f32 v[36:37], v[36:37], v[2:3]
	v_pk_mul_f32 v[40:41], v[40:41], v[2:3]
	v_or_b32_e32 v2, s37, v175
	v_mov_b32_e32 v159, v158
	v_lshlrev_b32_e32 v138, 1, v2
	v_ashrrev_i32_e32 v157, 31, v156
	v_mov_b32_e32 v169, v168
	v_pk_mul_f32 v[34:35], v[34:35], v[158:159]
	v_pk_mul_f32 v[38:39], v[38:39], v[158:159]
	v_lshl_add_u64 v[158:159], s[44:45], 0, v[138:139]
	v_lshlrev_b64 v[2:3], 12, v[156:157]
	v_pk_mul_f32 v[14:15], v[14:15], v[168:169]
	v_pk_mul_f32 v[18:19], v[18:19], v[168:169]
	v_mov_b32_e32 v168, v166
	v_mov_b32_e32 v169, v166
	v_pk_mul_f32 v[166:167], v[6:7], v[166:167]
	v_lshl_add_u64 v[2:3], v[158:159], 0, v[2:3]
	v_cvt_pk_bf16_f32 v6, v126, v127
	v_pk_mul_f32 v[4:5], v[4:5], v[168:169]
	v_pk_mul_f32 v[168:169], v[8:9], v[168:169]
	v_cvt_pk_bf16_f32 v7, v128, v129
	v_cvt_pk_bf16_f32 v8, v122, v123
	v_cvt_pk_bf16_f32 v9, v124, v125
	global_store_dwordx4 v[2:3], v[6:9], off
	v_mov_b32_e32 v161, v160
	v_pk_mul_f32 v[46:47], v[46:47], v[160:161]
	v_cvt_pk_bf16_f32 v6, v38, v39
	v_cvt_pk_bf16_f32 v7, v40, v41
	v_cvt_pk_bf16_f32 v8, v34, v35
	v_cvt_pk_bf16_f32 v9, v36, v37
	global_store_dwordx4 v[2:3], v[6:9], off offset:256
	v_pk_mul_f32 v[42:43], v[42:43], v[160:161]
	v_mov_b32_e32 v163, v162
	v_or_b32_e32 v6, 16, v156
	v_ashrrev_i32_e32 v7, 31, v6
	v_lshlrev_b64 v[6:7], 12, v[6:7]
	v_lshl_add_u64 v[34:35], v[158:159], 0, v[6:7]
	v_cvt_pk_bf16_f32 v6, v118, v119
	v_cvt_pk_bf16_f32 v7, v120, v121
	v_cvt_pk_bf16_f32 v8, v114, v115
	v_cvt_pk_bf16_f32 v9, v116, v117
	global_store_dwordx4 v[34:35], v[6:9], off
	v_pk_mul_f32 v[54:55], v[54:55], v[162:163]
	v_pk_mul_f32 v[50:51], v[50:51], v[162:163]
	v_cvt_pk_bf16_f32 v6, v46, v47
	v_cvt_pk_bf16_f32 v7, v48, v49
	v_cvt_pk_bf16_f32 v8, v42, v43
	v_cvt_pk_bf16_f32 v9, v44, v45
	global_store_dwordx4 v[34:35], v[6:9], off offset:256
	v_mov_b32_e32 v165, v164
	s_mov_b32 s37, 0x80000
	v_or_b32_e32 v6, 32, v156
	v_ashrrev_i32_e32 v7, 31, v6
	v_lshlrev_b64 v[6:7], 12, v[6:7]
	v_lshl_add_u64 v[34:35], v[158:159], 0, v[6:7]
	v_cvt_pk_bf16_f32 v6, v110, v111
	v_cvt_pk_bf16_f32 v7, v112, v113
	v_cvt_pk_bf16_f32 v8, v106, v107
	v_cvt_pk_bf16_f32 v9, v108, v109
	global_store_dwordx4 v[34:35], v[6:9], off
	v_pk_mul_f32 v[58:59], v[58:59], v[164:165]
	v_pk_mul_f32 v[62:63], v[62:63], v[164:165]
	v_cvt_pk_bf16_f32 v6, v54, v55
	v_cvt_pk_bf16_f32 v7, v56, v57
	v_cvt_pk_bf16_f32 v8, v50, v51
	v_cvt_pk_bf16_f32 v9, v52, v53
	global_store_dwordx4 v[34:35], v[6:9], off offset:256
	s_mov_b64 s[42:43], 0x80000
	v_add_co_u32_e32 v36, vcc, s37, v2
	v_or_b32_e32 v6, 48, v156
	v_ashrrev_i32_e32 v7, 31, v6
	v_lshlrev_b64 v[6:7], 12, v[6:7]
	v_lshl_add_u64 v[34:35], v[158:159], 0, v[6:7]
	v_cvt_pk_bf16_f32 v6, v102, v103
	v_cvt_pk_bf16_f32 v7, v104, v105
	v_cvt_pk_bf16_f32 v8, v98, v99
	v_cvt_pk_bf16_f32 v9, v100, v101
	global_store_dwordx4 v[34:35], v[6:9], off
	v_addc_co_u32_e32 v37, vcc, 0, v3, vcc
	s_nop 0
	v_cvt_pk_bf16_f32 v6, v62, v63
	v_cvt_pk_bf16_f32 v7, v64, v65
	v_cvt_pk_bf16_f32 v8, v58, v59
	v_cvt_pk_bf16_f32 v9, v60, v61
	global_store_dwordx4 v[34:35], v[6:9], off offset:256
	v_lshl_add_u64 v[34:35], v[2:3], 0, s[42:43]
	s_mov_b32 s37, 0x90000
	v_cvt_pk_bf16_f32 v6, v94, v95
	v_cvt_pk_bf16_f32 v7, v96, v97
	v_cvt_pk_bf16_f32 v8, v90, v91
	v_cvt_pk_bf16_f32 v9, v92, v93
	global_store_dwordx4 v[36:37], v[6:9], off
	s_mov_b64 s[42:43], 0x90000
	v_pk_mul_f32 v[24:25], v[24:25], v[172:173]
	v_cvt_pk_bf16_f32 v6, v166, v167
	v_cvt_pk_bf16_f32 v7, v168, v169
	v_cvt_pk_bf16_f32 v8, v170, v171
	v_cvt_pk_bf16_f32 v9, v4, v5
	global_store_dwordx4 v[34:35], v[6:9], off offset:256
	v_add_co_u32_e32 v34, vcc, s37, v2
	v_cvt_pk_bf16_f32 v4, v86, v87
	v_cvt_pk_bf16_f32 v5, v88, v89
	s_nop 0
	v_cvt_pk_bf16_f32 v6, v82, v83
	v_cvt_pk_bf16_f32 v7, v84, v85
	s_nop 0
	v_addc_co_u32_e32 v35, vcc, 0, v3, vcc
	s_mov_b32 s37, 0xa0000
	v_lshl_add_u64 v[8:9], v[2:3], 0, s[42:43]
	global_store_dwordx4 v[34:35], v[4:7], off
	s_mov_b64 s[42:43], 0xa0000
	v_pk_mul_f32 v[28:29], v[28:29], v[172:173]
	v_cvt_pk_bf16_f32 v4, v18, v19
	v_cvt_pk_bf16_f32 v5, v20, v21
	v_cvt_pk_bf16_f32 v6, v14, v15
	v_cvt_pk_bf16_f32 v7, v16, v17
	v_add_co_u32_e32 v14, vcc, s37, v2
	global_store_dwordx4 v[8:9], v[4:7], off offset:256
	v_lshl_add_u64 v[8:9], v[2:3], 0, s[42:43]
	v_addc_co_u32_e32 v15, vcc, 0, v3, vcc
	v_cvt_pk_bf16_f32 v4, v78, v79
	v_cvt_pk_bf16_f32 v5, v80, v81
	v_cvt_pk_bf16_f32 v6, v74, v75
	v_cvt_pk_bf16_f32 v7, v76, v77
	global_store_dwordx4 v[14:15], v[4:7], off
	v_pk_mul_f32 v[12:13], v[12:13], v[180:181]
	v_pk_mul_f32 v[32:33], v[32:33], v[180:181]
	v_cvt_pk_bf16_f32 v4, v26, v27
	v_cvt_pk_bf16_f32 v5, v28, v29
	v_cvt_pk_bf16_f32 v6, v22, v23
	v_cvt_pk_bf16_f32 v7, v24, v25
	global_store_dwordx4 v[8:9], v[4:7], off offset:256
	v_lshl_add_u64 v[8:9], v[2:3], 0, s[18:19]
	v_add_co_u32_e32 v2, vcc, s67, v2
	v_cvt_pk_bf16_f32 v4, v70, v71
	v_cvt_pk_bf16_f32 v5, v72, v73
	v_cvt_pk_bf16_f32 v6, v66, v67
	v_cvt_pk_bf16_f32 v7, v68, v69
	s_nop 1
	v_addc_co_u32_e32 v3, vcc, 0, v3, vcc
	global_store_dwordx4 v[2:3], v[4:7], off
	v_cvt_pk_bf16_f32 v2, v30, v31
	v_cvt_pk_bf16_f32 v3, v32, v33
	s_mov_b64 s[44:45], 0
	s_nop 0
	v_cvt_pk_bf16_f32 v4, v10, v11
	v_cvt_pk_bf16_f32 v5, v12, v13
	global_store_dwordx4 v[8:9], v[2:5], off offset:256
